# v12 + nt policy also on the P10 background down-weight conversion loads and stores
# speedup vs baseline: 1.0358x; 1.0007x over previous
.LBB0_1699:
	v_lshrrev_b32_e32 v131, 4, v196
	v_mul_u32_u24_e32 v2, s4, v131
	v_and_b32_e32 v130, 60, v194
	v_mov_b32_e32 v133, 0
	v_lshlrev_b32_e32 v132, 2, v2
	v_lshl_add_u64 v[2:3], s[2:3], 0, v[132:133]
	v_lshlrev_b32_e32 v132, 2, v130
	v_or_b32_e32 v135, 4, v131
	v_lshl_add_u64 v[10:11], v[2:3], 0, v[132:133]
	v_mul_u32_u24_e32 v2, s4, v135
	v_lshlrev_b32_e32 v2, 2, v2
	v_mov_b32_e32 v3, v133
	v_lshl_add_u64 v[2:3], s[2:3], 0, v[2:3]
	v_or_b32_e32 v139, 8, v131
	v_lshl_add_u64 v[12:13], v[2:3], 0, v[132:133]
	global_load_dwordx4 v[2:5], v[10:11], off nt
	global_load_dwordx4 v[6:9], v[12:13], off nt
	v_mul_u32_u24_e32 v10, s4, v139
	v_lshlrev_b32_e32 v10, 2, v10
	v_mov_b32_e32 v11, v133
	v_lshl_add_u64 v[10:11], s[2:3], 0, v[10:11]
	v_or_b32_e32 v141, 12, v131
	v_lshl_add_u64 v[18:19], v[10:11], 0, v[132:133]
	v_mul_u32_u24_e32 v10, s4, v141
	v_lshlrev_b32_e32 v10, 2, v10
	v_mov_b32_e32 v11, v133
	v_lshl_add_u64 v[10:11], s[2:3], 0, v[10:11]
	v_or_b32_e32 v143, 16, v131
	v_lshl_add_u64 v[20:21], v[10:11], 0, v[132:133]
	global_load_dwordx4 v[10:13], v[18:19], off nt
	global_load_dwordx4 v[14:17], v[20:21], off nt
	v_mul_u32_u24_e32 v18, s4, v143
	v_lshlrev_b32_e32 v18, 2, v18
	v_mov_b32_e32 v19, v133
	v_lshl_add_u64 v[18:19], s[2:3], 0, v[18:19]
	v_or_b32_e32 v145, 20, v131
	v_lshl_add_u64 v[26:27], v[18:19], 0, v[132:133]
	v_mul_u32_u24_e32 v18, s4, v145
	v_lshlrev_b32_e32 v18, 2, v18
	v_mov_b32_e32 v19, v133
	v_lshl_add_u64 v[18:19], s[2:3], 0, v[18:19]
	v_or_b32_e32 v147, 24, v131
	v_lshl_add_u64 v[28:29], v[18:19], 0, v[132:133]
	global_load_dwordx4 v[18:21], v[26:27], off nt
	global_load_dwordx4 v[22:25], v[28:29], off nt
	v_mul_u32_u24_e32 v26, s4, v147
	v_lshlrev_b32_e32 v26, 2, v26
	v_mov_b32_e32 v27, v133
	v_lshl_add_u64 v[26:27], s[2:3], 0, v[26:27]
	v_or_b32_e32 v149, 28, v131
	v_lshl_add_u64 v[34:35], v[26:27], 0, v[132:133]
	v_mul_u32_u24_e32 v26, s4, v149
	v_lshlrev_b32_e32 v26, 2, v26
	v_mov_b32_e32 v27, v133
	v_lshl_add_u64 v[26:27], s[2:3], 0, v[26:27]
	v_or_b32_e32 v151, 32, v131
	v_lshl_add_u64 v[36:37], v[26:27], 0, v[132:133]
	global_load_dwordx4 v[26:29], v[34:35], off nt
	global_load_dwordx4 v[30:33], v[36:37], off nt
	v_mul_u32_u24_e32 v34, s4, v151
	v_lshlrev_b32_e32 v34, 2, v34
	v_mov_b32_e32 v35, v133
	v_lshl_add_u64 v[34:35], s[2:3], 0, v[34:35]
	v_or_b32_e32 v170, 36, v131
	v_lshl_add_u64 v[42:43], v[34:35], 0, v[132:133]
	v_mul_u32_u24_e32 v34, s4, v170
	v_lshlrev_b32_e32 v34, 2, v34
	v_mov_b32_e32 v35, v133
	v_lshl_add_u64 v[34:35], s[2:3], 0, v[34:35]
	v_or_b32_e32 v171, 40, v131
	v_lshl_add_u64 v[44:45], v[34:35], 0, v[132:133]
	global_load_dwordx4 v[34:37], v[42:43], off nt
	global_load_dwordx4 v[38:41], v[44:45], off nt
	v_mul_u32_u24_e32 v42, s4, v171
	v_lshlrev_b32_e32 v42, 2, v42
	v_mov_b32_e32 v43, v133
	v_lshl_add_u64 v[42:43], s[2:3], 0, v[42:43]
	v_or_b32_e32 v172, 44, v131
	v_lshl_add_u64 v[50:51], v[42:43], 0, v[132:133]
	v_mul_u32_u24_e32 v42, s4, v172
	v_lshlrev_b32_e32 v42, 2, v42
	v_mov_b32_e32 v43, v133
	v_lshl_add_u64 v[42:43], s[2:3], 0, v[42:43]
	v_or_b32_e32 v173, 48, v131
	v_lshl_add_u64 v[52:53], v[42:43], 0, v[132:133]
	global_load_dwordx4 v[42:45], v[50:51], off nt
	global_load_dwordx4 v[46:49], v[52:53], off nt
	v_mul_u32_u24_e32 v50, s4, v173
	v_lshlrev_b32_e32 v50, 2, v50
	v_mov_b32_e32 v51, v133
	v_lshl_add_u64 v[50:51], s[2:3], 0, v[50:51]
	v_or_b32_e32 v174, 52, v131
	v_lshl_add_u64 v[58:59], v[50:51], 0, v[132:133]
	v_mul_u32_u24_e32 v50, s4, v174
	v_lshlrev_b32_e32 v50, 2, v50
	v_mov_b32_e32 v51, v133
	v_lshl_add_u64 v[50:51], s[2:3], 0, v[50:51]
	v_or_b32_e32 v175, 56, v131
	v_lshl_add_u64 v[60:61], v[50:51], 0, v[132:133]
	global_load_dwordx4 v[50:53], v[58:59], off nt
	global_load_dwordx4 v[54:57], v[60:61], off nt
	v_mul_u32_u24_e32 v58, s4, v175
	v_or_b32_e32 v176, 60, v131
	v_lshlrev_b32_e32 v58, 2, v58
	v_mov_b32_e32 v59, v133
	v_mul_u32_u24_e32 v60, s4, v176
	v_lshl_add_u64 v[58:59], s[2:3], 0, v[58:59]
	v_lshlrev_b32_e32 v60, 2, v60
	v_mov_b32_e32 v61, v133
	v_lshl_add_u64 v[58:59], v[58:59], 0, v[132:133]
	v_lshl_add_u64 v[60:61], s[2:3], 0, v[60:61]
	v_lshl_add_u64 v[60:61], v[60:61], 0, v[132:133]
	global_load_dwordx4 v[66:69], v[58:59], off nt
	global_load_dwordx4 v[70:73], v[60:61], off nt
	s_mul_i32 s2, s88, 0x4100
	s_add_i32 s2, s2, 0
	s_bfe_u32 s20, s87, 0x10006
	s_add_u32 s21, s50, 0x14400000
	s_addc_u32 s22, s51, 0
	s_add_u32 s23, s50, 0x1600000
	s_addc_u32 s24, s51, 0
	s_add_u32 s25, s50, 0xe00000
	s_addc_u32 s26, s51, 0
	s_add_u32 s27, s50, 0xa00000
	s_addc_u32 s28, s51, 0
	v_and_b32_e32 v60, 7, v0
	v_lshrrev_b32_e32 v134, 3, v196
	s_add_u32 s30, s50, 0xd200000
	v_mul_u32_u24_e32 v61, 0x820, v60
	v_lshlrev_b32_e32 v62, 2, v134
	v_add_u32_e32 v58, s2, v132
	s_addc_u32 s33, s51, 0
	v_add3_u32 v177, s2, v61, v62
	s_lshl_b32 s2, s6, 3
	s_sub_i32 s34, 0, s2
	s_lshl_b32 s2, s86, 3
	s_add_i32 s35, s88, s2
	s_lshl_b32 s2, s52, 4
	s_lshl_b32 s3, s6, 4
	s_mul_i32 s6, s6, 24
	v_mul_u32_u24_e32 v59, 0x104, v131
	s_sub_i32 s36, s2, s3
	s_sub_i32 s37, s2, s6
	s_lshl_b32 s2, s52, 3
	v_lshlrev_b32_e32 v136, 3, v60
	v_mov_b32_e32 v137, v133
	v_or_b32_e32 v138, 8, v134
	v_or_b32_e32 v140, 16, v134
	v_or_b32_e32 v142, 24, v134
	v_or_b32_e32 v144, 32, v134
	v_or_b32_e32 v146, 40, v134
	v_or_b32_e32 v148, 48, v134
	v_or_b32_e32 v150, 56, v134
	v_lshlrev_b32_e32 v152, 4, v60
	v_mov_b32_e32 v153, v133
	s_sub_i32 s38, s2, s3
	s_add_i32 s39, 0, 0x27ea8
	s_add_i32 s40, 0, 0x27e90
	s_movk_i32 s41, 0x98
	s_movk_i32 s42, 0x88
	s_add_i32 s43, 0, 0x27e60
	s_add_i32 s44, 0, 0x27e58
	s_add_i32 s45, 0, 0x27e50
	s_add_i32 s46, 0, 0x27e30
	s_mov_b32 s47, 0xc3e00000
	v_add_u32_e32 v178, v58, v59
	v_mov_b32_e32 v179, 0x43e00000
	s_mov_b32 s57, s55
	s_mov_b32 s56, s54
	s_mov_b64 s[2:3], s[0:1]
	s_branch .LBB0_1703
.LBB0_1700:
	ds_read2_b32 v[158:159], v181 offset0:56 offset1:65
	ds_read2_b32 v[160:161], v181 offset0:121 offset1:130
	ds_read2_b32 v[162:163], v181 offset0:186 offset1:195
	ds_read2_b32 v[164:165], v182 offset0:123 offset1:132
	ds_read2_b32 v[166:167], v180 offset0:60 offset1:69
	ds_read2_b32 v[168:169], v180 offset0:125 offset1:134
	ds_read2_b32 v[182:183], v180 offset0:190 offset1:199
	v_mov_b64_e32 v[184:185], s[2:3]
	ds_read2_b32 v[188:189], v181 offset0:8 offset1:16
	ds_read2_b32 v[190:191], v181 offset0:73 offset1:81
	ds_read2_b32 v[192:193], v181 offset0:138 offset1:146
	ds_read2_b32 v[202:203], v181 offset0:203 offset1:211
	ds_read2_b32 v[204:205], v180 offset0:12 offset1:20
	ds_read2_b32 v[206:207], v180 offset0:77 offset1:85
	ds_read2_b32 v[208:209], v180 offset0:142 offset1:150
	ds_read2_b32 v[210:211], v180 offset0:207 offset1:215
	v_mad_u64_u32 v[186:187], s[4:5], s56, v134, v[184:185]
	v_lshl_add_u64 v[186:187], v[186:187], 0, v[152:153]
	s_waitcnt lgkmcnt(14)
	v_cvt_pk_bf16_f32 v154, v132, v159
	s_waitcnt lgkmcnt(12)
	v_cvt_pk_bf16_f32 v155, v161, v163
	s_waitcnt lgkmcnt(10)
	v_cvt_pk_bf16_f32 v156, v165, v167
	s_waitcnt lgkmcnt(8)
	v_cvt_pk_bf16_f32 v157, v169, v183
	global_store_dwordx4 v[186:187], v[154:157], off nt
	v_mad_u64_u32 v[186:187], s[4:5], s56, v138, v[184:185]
	v_lshl_add_u64 v[186:187], v[186:187], 0, v[152:153]
	s_waitcnt lgkmcnt(6)
	v_cvt_pk_bf16_f32 v154, v188, v190
	s_waitcnt lgkmcnt(4)
	v_cvt_pk_bf16_f32 v155, v192, v202
	s_waitcnt lgkmcnt(2)
	v_cvt_pk_bf16_f32 v156, v204, v206
	s_waitcnt lgkmcnt(0)
	v_cvt_pk_bf16_f32 v157, v208, v210
	global_store_dwordx4 v[186:187], v[154:157], off nt
	v_mad_u64_u32 v[186:187], s[4:5], s56, v140, v[184:185]
	s_nop 0
	v_cvt_pk_bf16_f32 v154, v189, v191
	v_cvt_pk_bf16_f32 v155, v193, v203
	v_cvt_pk_bf16_f32 v156, v205, v207
	v_cvt_pk_bf16_f32 v157, v209, v211
	ds_read2_b32 v[188:189], v181 offset0:24 offset1:32
	ds_read2_b32 v[190:191], v181 offset0:89 offset1:97
	ds_read2_b32 v[192:193], v181 offset0:154 offset1:162
	ds_read2_b32 v[202:203], v181 offset0:219 offset1:227
	ds_read2_b32 v[204:205], v180 offset0:28 offset1:36
	ds_read2_b32 v[206:207], v180 offset0:93 offset1:101
	ds_read2_b32 v[208:209], v180 offset0:158 offset1:166
	ds_read2_b32 v[210:211], v180 offset0:223 offset1:231
	v_lshl_add_u64 v[186:187], v[186:187], 0, v[152:153]
	global_store_dwordx4 v[186:187], v[154:157], off nt
	v_mad_u64_u32 v[186:187], s[4:5], s56, v142, v[184:185]
	v_lshl_add_u64 v[186:187], v[186:187], 0, v[152:153]
	s_waitcnt lgkmcnt(6)
	v_cvt_pk_bf16_f32 v154, v188, v190
	s_waitcnt lgkmcnt(4)
	v_cvt_pk_bf16_f32 v155, v192, v202
	s_waitcnt lgkmcnt(2)
	v_cvt_pk_bf16_f32 v156, v204, v206
	s_waitcnt lgkmcnt(0)
	v_cvt_pk_bf16_f32 v157, v208, v210
	global_store_dwordx4 v[186:187], v[154:157], off nt
	v_mad_u64_u32 v[186:187], s[4:5], s56, v144, v[184:185]
	s_nop 0
	v_cvt_pk_bf16_f32 v154, v189, v191
	v_cvt_pk_bf16_f32 v155, v193, v203
	v_cvt_pk_bf16_f32 v156, v205, v207
	v_cvt_pk_bf16_f32 v157, v209, v211
	ds_read2_b32 v[188:189], v181 offset0:40 offset1:48
	ds_read2_b32 v[190:191], v181 offset0:105 offset1:113
	ds_read2_b32 v[192:193], v181 offset0:170 offset1:178
	ds_read2_b32 v[202:203], v181 offset0:235 offset1:243
	ds_read2_b32 v[204:205], v180 offset0:44 offset1:52
	ds_read2_b32 v[206:207], v180 offset0:109 offset1:117
	ds_read2_b32 v[208:209], v180 offset0:174 offset1:182
	ds_read2_b32 v[180:181], v180 offset0:239 offset1:247
	v_lshl_add_u64 v[186:187], v[186:187], 0, v[152:153]
	global_store_dwordx4 v[186:187], v[154:157], off nt
	v_mad_u64_u32 v[186:187], s[4:5], s56, v146, v[184:185]
	s_waitcnt lgkmcnt(0)
	v_cvt_pk_bf16_f32 v157, v208, v180
	v_lshl_add_u64 v[186:187], v[186:187], 0, v[152:153]
	v_cvt_pk_bf16_f32 v154, v188, v190
	v_cvt_pk_bf16_f32 v155, v192, v202
	v_cvt_pk_bf16_f32 v156, v204, v206
	global_store_dwordx4 v[186:187], v[154:157], off nt
	ds_read_b32 v132, v177 offset:18428
	s_nop 0
	v_cvt_pk_bf16_f32 v157, v209, v181
	v_mad_u64_u32 v[180:181], s[4:5], s56, v148, v[184:185]
	v_cvt_pk_bf16_f32 v154, v189, v191
	v_lshl_add_u64 v[180:181], v[180:181], 0, v[152:153]
	v_cvt_pk_bf16_f32 v155, v193, v203
	v_cvt_pk_bf16_f32 v156, v205, v207
	global_store_dwordx4 v[180:181], v[154:157], off nt
	s_nop 1
	v_cvt_pk_bf16_f32 v154, v158, v160
	v_mad_u64_u32 v[158:159], s[4:5], s56, v150, v[184:185]
	v_lshl_add_u64 v[158:159], v[158:159], 0, v[152:153]
	v_cvt_pk_bf16_f32 v155, v162, v164
	v_cvt_pk_bf16_f32 v156, v166, v168
	s_waitcnt lgkmcnt(0)
	v_cvt_pk_bf16_f32 v157, v182, v132
	global_store_dwordx4 v[158:159], v[154:157], off nt

.LBB0_1731:
	v_mul_u32_u24_e32 v58, s8, v131
	v_mul_u32_u24_e32 v60, s8, v135
	v_mul_u32_u24_e32 v74, s8, v139
	v_mul_u32_u24_e32 v76, s8, v141
	v_mul_u32_u24_e32 v82, s8, v143
	v_mul_u32_u24_e32 v84, s8, v145
	v_mul_u32_u24_e32 v90, s8, v147
	v_mul_u32_u24_e32 v92, s8, v149
	v_mul_u32_u24_e32 v98, s8, v151
	v_mul_u32_u24_e32 v100, s8, v170
	v_mul_u32_u24_e32 v106, s8, v171
	v_mul_u32_u24_e32 v108, s8, v172
	v_mul_u32_u24_e32 v114, s8, v173
	v_mul_u32_u24_e32 v116, s8, v174
	v_mul_u32_u24_e32 v122, s8, v175
	v_mul_u32_u24_e32 v124, s8, v176
	s_waitcnt lgkmcnt(0)
	v_lshlrev_b32_e32 v132, 2, v58
	v_lshlrev_b32_e32 v60, 2, v60
	v_mov_b32_e32 v61, v133
	v_lshlrev_b32_e32 v74, 2, v74
	v_mov_b32_e32 v75, v133
	v_lshlrev_b32_e32 v76, 2, v76
	v_mov_b32_e32 v77, v133
	v_lshlrev_b32_e32 v82, 2, v82
	v_mov_b32_e32 v83, v133
	v_lshlrev_b32_e32 v84, 2, v84
	v_mov_b32_e32 v85, v133
	v_lshlrev_b32_e32 v90, 2, v90
	v_mov_b32_e32 v91, v133
	v_lshlrev_b32_e32 v92, 2, v92
	v_mov_b32_e32 v93, v133
	v_lshlrev_b32_e32 v98, 2, v98
	v_mov_b32_e32 v99, v133
	v_lshlrev_b32_e32 v100, 2, v100
	v_mov_b32_e32 v101, v133
	v_lshlrev_b32_e32 v106, 2, v106
	v_mov_b32_e32 v107, v133
	v_lshlrev_b32_e32 v108, 2, v108
	v_mov_b32_e32 v109, v133
	v_lshlrev_b32_e32 v114, 2, v114
	v_mov_b32_e32 v115, v133
	v_lshlrev_b32_e32 v116, 2, v116
	v_mov_b32_e32 v117, v133
	v_lshlrev_b32_e32 v122, 2, v122
	v_mov_b32_e32 v123, v133
	v_lshlrev_b32_e32 v124, 2, v124
	v_mov_b32_e32 v125, v133
	v_lshl_add_u64 v[58:59], s[6:7], 0, v[132:133]
	v_lshlrev_b32_e32 v132, 2, v130
	v_lshl_add_u64 v[60:61], s[6:7], 0, v[60:61]
	v_lshl_add_u64 v[74:75], s[6:7], 0, v[74:75]
	v_lshl_add_u64 v[76:77], s[6:7], 0, v[76:77]
	v_lshl_add_u64 v[82:83], s[6:7], 0, v[82:83]
	v_lshl_add_u64 v[84:85], s[6:7], 0, v[84:85]
	v_lshl_add_u64 v[90:91], s[6:7], 0, v[90:91]
	v_lshl_add_u64 v[92:93], s[6:7], 0, v[92:93]
	v_lshl_add_u64 v[98:99], s[6:7], 0, v[98:99]
	v_lshl_add_u64 v[100:101], s[6:7], 0, v[100:101]
	v_lshl_add_u64 v[106:107], s[6:7], 0, v[106:107]
	v_lshl_add_u64 v[108:109], s[6:7], 0, v[108:109]
	v_lshl_add_u64 v[114:115], s[6:7], 0, v[114:115]
	v_lshl_add_u64 v[116:117], s[6:7], 0, v[116:117]
	v_lshl_add_u64 v[122:123], s[6:7], 0, v[122:123]
	v_lshl_add_u64 v[124:125], s[6:7], 0, v[124:125]
	v_lshl_add_u64 v[58:59], v[58:59], 0, v[132:133]
	v_lshl_add_u64 v[60:61], v[60:61], 0, v[132:133]
	v_lshl_add_u64 v[74:75], v[74:75], 0, v[132:133]
	v_lshl_add_u64 v[76:77], v[76:77], 0, v[132:133]
	v_lshl_add_u64 v[82:83], v[82:83], 0, v[132:133]
	v_lshl_add_u64 v[84:85], v[84:85], 0, v[132:133]
	v_lshl_add_u64 v[90:91], v[90:91], 0, v[132:133]
	v_lshl_add_u64 v[92:93], v[92:93], 0, v[132:133]
	v_lshl_add_u64 v[98:99], v[98:99], 0, v[132:133]
	v_lshl_add_u64 v[100:101], v[100:101], 0, v[132:133]
	v_lshl_add_u64 v[106:107], v[106:107], 0, v[132:133]
	v_lshl_add_u64 v[108:109], v[108:109], 0, v[132:133]
	v_lshl_add_u64 v[114:115], v[114:115], 0, v[132:133]
	v_lshl_add_u64 v[116:117], v[116:117], 0, v[132:133]
	v_lshl_add_u64 v[122:123], v[122:123], 0, v[132:133]
	v_lshl_add_u64 v[124:125], v[124:125], 0, v[132:133]
	global_load_dwordx4 v[62:65], v[58:59], off nt
	s_nop 0
	global_load_dwordx4 v[58:61], v[60:61], off nt
	s_nop 0
	global_load_dwordx4 v[78:81], v[74:75], off nt
	s_nop 0
	global_load_dwordx4 v[74:77], v[76:77], off nt
	s_nop 0
	global_load_dwordx4 v[86:89], v[82:83], off nt
	s_nop 0
	global_load_dwordx4 v[82:85], v[84:85], off nt
	s_nop 0
	global_load_dwordx4 v[94:97], v[90:91], off nt
	s_nop 0
	global_load_dwordx4 v[90:93], v[92:93], off nt
	s_nop 0
	global_load_dwordx4 v[102:105], v[98:99], off nt
	s_nop 0
	global_load_dwordx4 v[98:101], v[100:101], off nt
	s_nop 0
	global_load_dwordx4 v[110:113], v[106:107], off nt
	s_nop 0
	global_load_dwordx4 v[106:109], v[108:109], off nt
	s_nop 0
	global_load_dwordx4 v[118:121], v[114:115], off nt
	s_nop 0
	global_load_dwordx4 v[114:117], v[116:117], off nt
	s_nop 0
	global_load_dwordx4 v[126:129], v[122:123], off nt
	s_nop 0
	global_load_dwordx4 v[122:125], v[124:125], off nt
.LBB0_1732:
	v_add_u32_e32 v183, 0x4000, v178
	v_add_u32_e32 v184, 0x4008, v178
	v_add_u32_e32 v185, 0x4410, v178
	v_add_u32_e32 v186, 0x4418, v178
	v_add_u32_e32 v187, 0x4820, v178
	v_add_u32_e32 v188, 0x4828, v178
	v_add_u32_e32 v189, 0x4c30, v178
	v_add_u32_e32 v190, 0x4c38, v178
	v_add_u32_e32 v191, 0x5040, v178
	v_add_u32_e32 v192, 0x5048, v178
	v_add_u32_e32 v193, 0x5450, v178
	v_add_u32_e32 v195, 0x5458, v178
	v_add_u32_e32 v199, 0x5860, v178
	v_add_u32_e32 v201, 0x5868, v178
	v_add_u32_e32 v202, 0x5c70, v178
	v_add_u32_e32 v203, 0x5c78, v178
	v_add_u32_e32 v204, 0x6080, v178
	v_add_u32_e32 v205, 0x6088, v178
	v_add_u32_e32 v206, 0x6490, v178
	v_add_u32_e32 v207, 0x6498, v178
	v_add_u32_e32 v208, 0x68a0, v178
	v_add_u32_e32 v209, 0x68a8, v178
	v_add_u32_e32 v210, 0x6cb0, v178
	v_add_u32_e32 v211, 0x6cb8, v178
	v_add_u32_e32 v212, 0x70c0, v178
	v_add_u32_e32 v213, 0x70c8, v178
	v_add_u32_e32 v214, 0x74d0, v178
	v_add_u32_e32 v215, 0x74d8, v178
	v_add_u32_e32 v216, 0x78e0, v178
	v_add_u32_e32 v217, 0x78e8, v178
	v_add_u32_e32 v218, 0x7cf0, v178
	v_add_u32_e32 v219, 0x7cf8, v178
	s_waitcnt vmcnt(15)
	ds_write2_b32 v183, v2, v3 offset1:1
	ds_write2_b32 v184, v4, v5 offset1:1
	s_waitcnt vmcnt(14)
	ds_write2_b32 v185, v6, v7 offset1:1
	ds_write2_b32 v186, v8, v9 offset1:1
	s_waitcnt vmcnt(13)
	ds_write2_b32 v187, v10, v11 offset1:1
	ds_write2_b32 v188, v12, v13 offset1:1
	s_waitcnt vmcnt(12)
	ds_write2_b32 v189, v14, v15 offset1:1
	ds_write2_b32 v190, v16, v17 offset1:1
	s_waitcnt vmcnt(11)
	ds_write2_b32 v191, v18, v19 offset1:1
	ds_write2_b32 v192, v20, v21 offset1:1
	s_waitcnt vmcnt(10)
	ds_write2_b32 v193, v22, v23 offset1:1
	ds_write2_b32 v195, v24, v25 offset1:1
	s_waitcnt vmcnt(9)
	ds_write2_b32 v199, v26, v27 offset1:1
	ds_write2_b32 v201, v28, v29 offset1:1
	s_waitcnt vmcnt(8)
	ds_write2_b32 v202, v30, v31 offset1:1
	ds_write2_b32 v203, v32, v33 offset1:1
	s_waitcnt vmcnt(7)
	ds_write2_b32 v204, v34, v35 offset1:1
	ds_write2_b32 v205, v36, v37 offset1:1
	s_waitcnt vmcnt(6)
	ds_write2_b32 v206, v38, v39 offset1:1
	ds_write2_b32 v207, v40, v41 offset1:1
	s_waitcnt vmcnt(5)
	ds_write2_b32 v208, v42, v43 offset1:1
	ds_write2_b32 v209, v44, v45 offset1:1
	s_waitcnt vmcnt(4)
	ds_write2_b32 v210, v46, v47 offset1:1
	ds_write2_b32 v211, v48, v49 offset1:1
	s_waitcnt vmcnt(3)
	ds_write2_b32 v212, v50, v51 offset1:1
	ds_write2_b32 v213, v52, v53 offset1:1
	s_waitcnt vmcnt(2)
	ds_write2_b32 v214, v54, v55 offset1:1
	ds_write2_b32 v215, v56, v57 offset1:1
	s_waitcnt vmcnt(1)
	ds_write2_b32 v216, v66, v67 offset1:1
	ds_write2_b32 v217, v68, v69 offset1:1
	s_waitcnt vmcnt(0)
	ds_write2_b32 v218, v70, v71 offset1:1
	ds_write2_b32 v219, v72, v73 offset1:1
	s_waitcnt lgkmcnt(0)
	ds_read_b32 v132, v177 offset:16384
	v_cmp_eq_f32_e64 s[6:7], s55, 0
	s_and_b64 vcc, exec, s[6:7]
	v_add_u32_e32 v181, 0x4000, v177
	v_add_u32_e32 v182, 0x4200, v177
	v_add_u32_e32 v180, 0x4400, v177
	s_cbranch_vccnz .LBB0_1753
	ds_read2_b32 v[154:155], v181 offset0:56 offset1:65
	ds_read2_b32 v[156:157], v181 offset0:121 offset1:130
	ds_read2_b32 v[158:159], v181 offset0:186 offset1:195
	s_waitcnt lgkmcnt(3)
	v_mul_f32_e32 v160, s55, v132
	v_med3_f32 v160, v160, s47, v179
	s_waitcnt lgkmcnt(2)
	v_mul_f32_e32 v155, s55, v155
	v_med3_f32 v155, v155, s47, v179
	v_mov_b32_e32 v220, v133
	v_cvt_pk_fp8_f32 v220, v160, v155
	ds_read2_b32 v[164:165], v182 offset0:123 offset1:132
	ds_read2_b32 v[160:161], v180 offset0:60 offset1:69
	ds_read2_b32 v[162:163], v180 offset0:125 offset1:134
	s_waitcnt lgkmcnt(4)
	v_mul_f32_e32 v157, s55, v157
	s_waitcnt lgkmcnt(3)
	v_mul_f32_e32 v159, s55, v159
	v_med3_f32 v157, v157, s47, v179
	v_med3_f32 v155, v159, s47, v179
	ds_read2_b32 v[168:169], v180 offset0:190 offset1:199
	v_cvt_pk_fp8_f32 v220, v157, v155 op_sel:[0,0,1]
	s_waitcnt lgkmcnt(3)
	v_mul_f32_e32 v155, s55, v165
	s_waitcnt lgkmcnt(2)
	v_mul_f32_e32 v157, s55, v161
	v_med3_f32 v155, v155, s47, v179
	v_med3_f32 v157, v157, s47, v179
	v_mov_b32_e32 v221, v133
	v_cvt_pk_fp8_f32 v221, v155, v157
	s_waitcnt lgkmcnt(1)
	v_mul_f32_e32 v159, s55, v163
	s_waitcnt lgkmcnt(0)
	v_mul_f32_e32 v155, s55, v169
	v_med3_f32 v157, v159, s47, v179
	v_med3_f32 v155, v155, s47, v179
	v_cvt_pk_fp8_f32 v221, v157, v155 op_sel:[0,0,1]
	ds_read2_b32 v[230:231], v181 offset0:8 offset1:16
	ds_read2_b32 v[232:233], v181 offset0:73 offset1:81
	ds_read2_b32 v[234:235], v181 offset0:138 offset1:146
	ds_read2_b32 v[236:237], v181 offset0:203 offset1:211
	v_mov_b64_e32 v[166:167], s[0:1]
	v_mad_u64_u32 v[228:229], s[6:7], s54, v134, v[166:167]
	v_lshl_add_u64 v[228:229], v[228:229], 0, v[136:137]
	s_waitcnt lgkmcnt(3)
	v_mul_f32_e32 v155, s55, v230
	s_waitcnt lgkmcnt(2)
	v_mul_f32_e32 v157, s55, v232
	global_store_dwordx2 v[228:229], v[220:221], off nt
	v_med3_f32 v155, v155, s47, v179
	v_med3_f32 v157, v157, s47, v179
	v_mov_b32_e32 v220, v133
	v_cvt_pk_fp8_f32 v220, v155, v157
	ds_read2_b32 v[228:229], v180 offset0:12 offset1:20
	ds_read2_b32 v[238:239], v180 offset0:77 offset1:85
	ds_read2_b32 v[240:241], v180 offset0:142 offset1:150
	s_waitcnt lgkmcnt(4)
	v_mul_f32_e32 v159, s55, v234
	s_waitcnt lgkmcnt(3)
	v_mul_f32_e32 v161, s55, v236
	v_med3_f32 v159, v159, s47, v179
	v_med3_f32 v155, v161, s47, v179
	ds_read2_b32 v[242:243], v180 offset0:207 offset1:215
	v_cvt_pk_fp8_f32 v220, v159, v155 op_sel:[0,0,1]
	s_waitcnt lgkmcnt(3)
	v_mul_f32_e32 v155, s55, v228
	s_waitcnt lgkmcnt(2)
	v_mul_f32_e32 v157, s55, v238
	v_med3_f32 v155, v155, s47, v179
	v_med3_f32 v157, v157, s47, v179
	v_mov_b32_e32 v221, v133
	v_cvt_pk_fp8_f32 v221, v155, v157
	s_waitcnt lgkmcnt(1)
	v_mul_f32_e32 v159, s55, v240
	s_waitcnt lgkmcnt(0)
	v_mul_f32_e32 v155, s55, v242
	v_med3_f32 v157, v159, s47, v179
	v_med3_f32 v155, v155, s47, v179
	v_cvt_pk_fp8_f32 v221, v157, v155 op_sel:[0,0,1]
	v_mad_u64_u32 v[244:245], s[6:7], s54, v138, v[166:167]
	v_lshl_add_u64 v[244:245], v[244:245], 0, v[136:137]
	v_mul_f32_e32 v155, s55, v231
	v_mul_f32_e32 v157, s55, v233
	global_store_dwordx2 v[244:245], v[220:221], off nt
	v_med3_f32 v155, v155, s47, v179
	v_med3_f32 v157, v157, s47, v179
	v_mov_b32_e32 v220, v133
	v_cvt_pk_fp8_f32 v220, v155, v157
	v_mul_f32_e32 v159, s55, v235
	v_mul_f32_e32 v155, s55, v237
	v_med3_f32 v157, v159, s47, v179
	v_med3_f32 v155, v155, s47, v179
	v_cvt_pk_fp8_f32 v220, v157, v155 op_sel:[0,0,1]
	v_mul_f32_e32 v155, s55, v229
	v_mul_f32_e32 v157, s55, v239
	v_med3_f32 v155, v155, s47, v179
	v_med3_f32 v157, v157, s47, v179
	v_mov_b32_e32 v221, v133
	v_cvt_pk_fp8_f32 v221, v155, v157
	v_mul_f32_e32 v159, s55, v241
	v_mul_f32_e32 v155, s55, v243
	v_med3_f32 v157, v159, s47, v179
	v_med3_f32 v155, v155, s47, v179
	v_cvt_pk_fp8_f32 v221, v157, v155 op_sel:[0,0,1]
	ds_read2_b32 v[230:231], v181 offset0:24 offset1:32
	ds_read2_b32 v[232:233], v181 offset0:89 offset1:97
	ds_read2_b32 v[234:235], v181 offset0:154 offset1:162
	ds_read2_b32 v[236:237], v181 offset0:219 offset1:227
	v_mad_u64_u32 v[228:229], s[6:7], s54, v140, v[166:167]
	v_lshl_add_u64 v[228:229], v[228:229], 0, v[136:137]
	s_waitcnt lgkmcnt(3)
	v_mul_f32_e32 v155, s55, v230
	s_waitcnt lgkmcnt(2)
	v_mul_f32_e32 v157, s55, v232
	global_store_dwordx2 v[228:229], v[220:221], off nt
	v_med3_f32 v155, v155, s47, v179
	v_med3_f32 v157, v157, s47, v179
	v_mov_b32_e32 v220, v133
	v_cvt_pk_fp8_f32 v220, v155, v157
	ds_read2_b32 v[228:229], v180 offset0:28 offset1:36
	ds_read2_b32 v[238:239], v180 offset0:93 offset1:101
	ds_read2_b32 v[240:241], v180 offset0:158 offset1:166
	s_waitcnt lgkmcnt(4)
	v_mul_f32_e32 v159, s55, v234
	s_waitcnt lgkmcnt(3)
	v_mul_f32_e32 v161, s55, v236
	v_med3_f32 v159, v159, s47, v179
	v_med3_f32 v155, v161, s47, v179
	ds_read2_b32 v[242:243], v180 offset0:223 offset1:231
	v_cvt_pk_fp8_f32 v220, v159, v155 op_sel:[0,0,1]
	s_waitcnt lgkmcnt(3)
	v_mul_f32_e32 v155, s55, v228
	s_waitcnt lgkmcnt(2)
	v_mul_f32_e32 v157, s55, v238
	v_med3_f32 v155, v155, s47, v179
	v_med3_f32 v157, v157, s47, v179
	v_mov_b32_e32 v221, v133
	v_cvt_pk_fp8_f32 v221, v155, v157
	s_waitcnt lgkmcnt(1)
	v_mul_f32_e32 v159, s55, v240
	s_waitcnt lgkmcnt(0)
	v_mul_f32_e32 v155, s55, v242
	v_med3_f32 v157, v159, s47, v179
	v_med3_f32 v155, v155, s47, v179
	v_cvt_pk_fp8_f32 v221, v157, v155 op_sel:[0,0,1]
	v_mad_u64_u32 v[244:245], s[6:7], s54, v142, v[166:167]
	v_lshl_add_u64 v[244:245], v[244:245], 0, v[136:137]
	v_mul_f32_e32 v155, s55, v231
	v_mul_f32_e32 v157, s55, v233
	global_store_dwordx2 v[244:245], v[220:221], off nt
	v_med3_f32 v155, v155, s47, v179
	v_med3_f32 v157, v157, s47, v179
	v_mov_b32_e32 v220, v133
	v_cvt_pk_fp8_f32 v220, v155, v157
	v_mul_f32_e32 v159, s55, v235
	v_mul_f32_e32 v155, s55, v237
	v_med3_f32 v157, v159, s47, v179
	v_med3_f32 v155, v155, s47, v179
	v_cvt_pk_fp8_f32 v220, v157, v155 op_sel:[0,0,1]
	v_mul_f32_e32 v155, s55, v229
	v_mul_f32_e32 v157, s55, v239
	v_med3_f32 v155, v155, s47, v179
	v_med3_f32 v157, v157, s47, v179
	v_mov_b32_e32 v221, v133
	v_cvt_pk_fp8_f32 v221, v155, v157
	v_mul_f32_e32 v159, s55, v241
	v_mul_f32_e32 v155, s55, v243
	v_med3_f32 v157, v159, s47, v179
	v_med3_f32 v155, v155, s47, v179
	v_cvt_pk_fp8_f32 v221, v157, v155 op_sel:[0,0,1]
	ds_read2_b32 v[230:231], v181 offset0:40 offset1:48
	ds_read2_b32 v[232:233], v181 offset0:105 offset1:113
	ds_read2_b32 v[234:235], v181 offset0:170 offset1:178
	ds_read2_b32 v[236:237], v181 offset0:235 offset1:243
	v_mad_u64_u32 v[228:229], s[6:7], s54, v144, v[166:167]
	v_lshl_add_u64 v[228:229], v[228:229], 0, v[136:137]
	s_waitcnt lgkmcnt(3)
	v_mul_f32_e32 v155, s55, v230
	s_waitcnt lgkmcnt(2)
	v_mul_f32_e32 v157, s55, v232
	global_store_dwordx2 v[228:229], v[220:221], off nt
	v_med3_f32 v155, v155, s47, v179
	v_med3_f32 v157, v157, s47, v179
	v_mov_b32_e32 v220, v133
	v_cvt_pk_fp8_f32 v220, v155, v157
	ds_read2_b32 v[228:229], v180 offset0:44 offset1:52
	ds_read2_b32 v[238:239], v180 offset0:109 offset1:117
	ds_read2_b32 v[240:241], v180 offset0:174 offset1:182
	s_waitcnt lgkmcnt(4)
	v_mul_f32_e32 v159, s55, v234
	s_waitcnt lgkmcnt(3)
	v_mul_f32_e32 v161, s55, v236
	v_med3_f32 v159, v159, s47, v179
	v_med3_f32 v155, v161, s47, v179
	ds_read2_b32 v[242:243], v180 offset0:239 offset1:247
	v_cvt_pk_fp8_f32 v220, v159, v155 op_sel:[0,0,1]
	s_waitcnt lgkmcnt(3)
	v_mul_f32_e32 v155, s55, v228
	s_waitcnt lgkmcnt(2)
	v_mul_f32_e32 v157, s55, v238
	v_med3_f32 v155, v155, s47, v179
	v_med3_f32 v157, v157, s47, v179
	v_mov_b32_e32 v221, v133
	v_cvt_pk_fp8_f32 v221, v155, v157
	s_waitcnt lgkmcnt(1)
	v_mul_f32_e32 v159, s55, v240
	s_waitcnt lgkmcnt(0)
	v_mul_f32_e32 v155, s55, v242
	v_med3_f32 v157, v159, s47, v179
	v_med3_f32 v155, v155, s47, v179
	v_cvt_pk_fp8_f32 v221, v157, v155 op_sel:[0,0,1]
	v_mad_u64_u32 v[244:245], s[6:7], s54, v146, v[166:167]
	v_lshl_add_u64 v[244:245], v[244:245], 0, v[136:137]
	v_mul_f32_e32 v155, s55, v231
	v_mul_f32_e32 v157, s55, v233
	global_store_dwordx2 v[244:245], v[220:221], off nt
	v_med3_f32 v155, v155, s47, v179
	v_med3_f32 v157, v157, s47, v179
	v_mov_b32_e32 v220, v133
	v_cvt_pk_fp8_f32 v220, v155, v157
	v_mul_f32_e32 v159, s55, v235
	v_mul_f32_e32 v155, s55, v237
	v_med3_f32 v157, v159, s47, v179
	v_med3_f32 v155, v155, s47, v179
	v_cvt_pk_fp8_f32 v220, v157, v155 op_sel:[0,0,1]
	v_mul_f32_e32 v155, s55, v229
	v_mul_f32_e32 v157, s55, v239
	v_med3_f32 v155, v155, s47, v179
	v_med3_f32 v157, v157, s47, v179
	v_mov_b32_e32 v221, v133
	v_cvt_pk_fp8_f32 v221, v155, v157
	v_mul_f32_e32 v159, s55, v241
	v_mul_f32_e32 v155, s55, v243
	v_med3_f32 v157, v159, s47, v179
	v_med3_f32 v155, v155, s47, v179
	v_cvt_pk_fp8_f32 v221, v157, v155 op_sel:[0,0,1]
	v_mul_f32_e32 v154, s55, v154
	v_mul_f32_e32 v155, s55, v156
	v_med3_f32 v157, v154, s47, v179
	v_med3_f32 v155, v155, s47, v179
	v_mov_b32_e32 v154, v133
	v_cvt_pk_fp8_f32 v154, v157, v155
	v_mul_f32_e32 v156, s55, v158
	v_mul_f32_e32 v155, s55, v164
	v_med3_f32 v156, v156, s47, v179
	v_med3_f32 v155, v155, s47, v179
	ds_read_b32 v158, v177 offset:18428
	v_cvt_pk_fp8_f32 v154, v156, v155 op_sel:[0,0,1]
	v_mul_f32_e32 v155, s55, v160
	v_mul_f32_e32 v156, s55, v162
	v_med3_f32 v159, v155, s47, v179
	v_med3_f32 v156, v156, s47, v179
	v_mov_b32_e32 v155, v133
	v_cvt_pk_fp8_f32 v155, v159, v156
	v_mul_f32_e32 v157, s55, v168
	s_waitcnt lgkmcnt(0)
	v_mul_f32_e32 v156, s55, v158
	v_med3_f32 v157, v157, s47, v179
	v_med3_f32 v156, v156, s47, v179
	v_cvt_pk_fp8_f32 v155, v157, v156 op_sel:[0,0,1]
	v_mad_u64_u32 v[228:229], s[6:7], s54, v148, v[166:167]
	v_mad_u64_u32 v[156:157], s[6:7], s54, v150, v[166:167]
	v_lshl_add_u64 v[228:229], v[228:229], 0, v[136:137]
	v_lshl_add_u64 v[156:157], v[156:157], 0, v[136:137]
	global_store_dwordx2 v[228:229], v[220:221], off nt
	global_store_dwordx2 v[156:157], v[154:155], off nt
	s_cbranch_execnz .LBB0_1735
.LBB0_1734:
	ds_read2_b32 v[158:159], v181 offset0:56 offset1:65
	ds_read2_b32 v[160:161], v181 offset0:121 offset1:130
	ds_read2_b32 v[162:163], v181 offset0:186 offset1:195
	ds_read2_b32 v[164:165], v182 offset0:123 offset1:132
	ds_read2_b32 v[166:167], v180 offset0:60 offset1:69
	ds_read2_b32 v[168:169], v180 offset0:125 offset1:134
	ds_read2_b32 v[220:221], v180 offset0:190 offset1:199
	v_mov_b64_e32 v[228:229], s[0:1]
	ds_read2_b32 v[232:233], v181 offset0:8 offset1:16
	ds_read2_b32 v[234:235], v181 offset0:73 offset1:81
	ds_read2_b32 v[236:237], v181 offset0:138 offset1:146
	ds_read2_b32 v[238:239], v181 offset0:203 offset1:211
	ds_read2_b32 v[240:241], v180 offset0:12 offset1:20
	ds_read2_b32 v[242:243], v180 offset0:77 offset1:85
	ds_read2_b32 v[244:245], v180 offset0:142 offset1:150
	ds_read2_b32 v[246:247], v180 offset0:207 offset1:215
	v_mad_u64_u32 v[230:231], s[6:7], s54, v134, v[228:229]
	v_lshl_add_u64 v[230:231], v[230:231], 0, v[152:153]
	s_waitcnt lgkmcnt(14)
	v_cvt_pk_bf16_f32 v154, v132, v159
	s_waitcnt lgkmcnt(12)
	v_cvt_pk_bf16_f32 v155, v161, v163
	s_waitcnt lgkmcnt(10)
	v_cvt_pk_bf16_f32 v156, v165, v167
	s_waitcnt lgkmcnt(8)
	v_cvt_pk_bf16_f32 v157, v169, v221
	global_store_dwordx4 v[230:231], v[154:157], off nt
	v_mad_u64_u32 v[230:231], s[6:7], s54, v138, v[228:229]
	v_lshl_add_u64 v[230:231], v[230:231], 0, v[152:153]
	s_waitcnt lgkmcnt(6)
	v_cvt_pk_bf16_f32 v154, v232, v234
	s_waitcnt lgkmcnt(4)
	v_cvt_pk_bf16_f32 v155, v236, v238
	s_waitcnt lgkmcnt(2)
	v_cvt_pk_bf16_f32 v156, v240, v242
	s_waitcnt lgkmcnt(0)
	v_cvt_pk_bf16_f32 v157, v244, v246
	global_store_dwordx4 v[230:231], v[154:157], off nt
	v_mad_u64_u32 v[230:231], s[6:7], s54, v140, v[228:229]
	s_nop 0
	v_cvt_pk_bf16_f32 v154, v233, v235
	v_cvt_pk_bf16_f32 v155, v237, v239
	v_cvt_pk_bf16_f32 v156, v241, v243
	v_cvt_pk_bf16_f32 v157, v245, v247
	ds_read2_b32 v[232:233], v181 offset0:24 offset1:32
	ds_read2_b32 v[234:235], v181 offset0:89 offset1:97
	ds_read2_b32 v[236:237], v181 offset0:154 offset1:162
	ds_read2_b32 v[238:239], v181 offset0:219 offset1:227
	ds_read2_b32 v[240:241], v180 offset0:28 offset1:36
	ds_read2_b32 v[242:243], v180 offset0:93 offset1:101
	ds_read2_b32 v[244:245], v180 offset0:158 offset1:166
	ds_read2_b32 v[246:247], v180 offset0:223 offset1:231
	v_lshl_add_u64 v[230:231], v[230:231], 0, v[152:153]
	global_store_dwordx4 v[230:231], v[154:157], off nt
	v_mad_u64_u32 v[230:231], s[6:7], s54, v142, v[228:229]
	v_lshl_add_u64 v[230:231], v[230:231], 0, v[152:153]
	s_waitcnt lgkmcnt(6)
	v_cvt_pk_bf16_f32 v154, v232, v234
	s_waitcnt lgkmcnt(4)
	v_cvt_pk_bf16_f32 v155, v236, v238
	s_waitcnt lgkmcnt(2)
	v_cvt_pk_bf16_f32 v156, v240, v242
	s_waitcnt lgkmcnt(0)
	v_cvt_pk_bf16_f32 v157, v244, v246
	global_store_dwordx4 v[230:231], v[154:157], off nt
	v_mad_u64_u32 v[230:231], s[6:7], s54, v144, v[228:229]
	s_nop 0
	v_cvt_pk_bf16_f32 v154, v233, v235
	v_cvt_pk_bf16_f32 v155, v237, v239
	v_cvt_pk_bf16_f32 v156, v241, v243
	v_cvt_pk_bf16_f32 v157, v245, v247
	ds_read2_b32 v[232:233], v181 offset0:40 offset1:48
	ds_read2_b32 v[234:235], v181 offset0:105 offset1:113
	ds_read2_b32 v[236:237], v181 offset0:170 offset1:178
	ds_read2_b32 v[238:239], v181 offset0:235 offset1:243
	ds_read2_b32 v[240:241], v180 offset0:44 offset1:52
	ds_read2_b32 v[242:243], v180 offset0:109 offset1:117
	ds_read2_b32 v[244:245], v180 offset0:174 offset1:182
	ds_read2_b32 v[246:247], v180 offset0:239 offset1:247
	v_lshl_add_u64 v[230:231], v[230:231], 0, v[152:153]
	global_store_dwordx4 v[230:231], v[154:157], off nt
	v_mad_u64_u32 v[230:231], s[6:7], s54, v146, v[228:229]
	v_lshl_add_u64 v[230:231], v[230:231], 0, v[152:153]
	s_waitcnt lgkmcnt(6)
	v_cvt_pk_bf16_f32 v154, v232, v234
	s_waitcnt lgkmcnt(4)
	v_cvt_pk_bf16_f32 v155, v236, v238
	s_waitcnt lgkmcnt(2)
	v_cvt_pk_bf16_f32 v156, v240, v242
	s_waitcnt lgkmcnt(0)
	v_cvt_pk_bf16_f32 v157, v244, v246
	global_store_dwordx4 v[230:231], v[154:157], off nt
	v_mad_u64_u32 v[230:231], s[6:7], s54, v148, v[228:229]
	s_nop 0
	v_cvt_pk_bf16_f32 v154, v233, v235
	v_lshl_add_u64 v[230:231], v[230:231], 0, v[152:153]
	v_cvt_pk_bf16_f32 v155, v237, v239
	v_cvt_pk_bf16_f32 v156, v241, v243
	v_cvt_pk_bf16_f32 v157, v245, v247
	global_store_dwordx4 v[230:231], v[154:157], off nt
	ds_read_b32 v132, v177 offset:18428
	s_nop 0
	v_cvt_pk_bf16_f32 v154, v158, v160
	v_mad_u64_u32 v[158:159], s[6:7], s54, v150, v[228:229]
	v_lshl_add_u64 v[158:159], v[158:159], 0, v[152:153]
	v_cvt_pk_bf16_f32 v155, v162, v164
	v_cvt_pk_bf16_f32 v156, v166, v168
	s_waitcnt lgkmcnt(0)
	v_cvt_pk_bf16_f32 v157, v220, v132
	global_store_dwordx4 v[158:159], v[154:157], off nt

.LBB0_1768:
	v_mul_u32_u24_e32 v2, s6, v131
	v_mul_u32_u24_e32 v4, s6, v135
	v_mul_u32_u24_e32 v10, s6, v139
	v_mul_u32_u24_e32 v12, s6, v141
	v_mul_u32_u24_e32 v18, s6, v143
	v_mul_u32_u24_e32 v20, s6, v145
	v_mul_u32_u24_e32 v26, s6, v147
	v_mul_u32_u24_e32 v28, s6, v149
	v_mul_u32_u24_e32 v34, s6, v151
	v_mul_u32_u24_e32 v36, s6, v170
	v_mul_u32_u24_e32 v42, s6, v171
	v_mul_u32_u24_e32 v44, s6, v172
	v_mul_u32_u24_e32 v50, s6, v173
	v_mul_u32_u24_e32 v52, s6, v174
	v_mul_u32_u24_e32 v66, s6, v175
	v_mul_u32_u24_e32 v68, s6, v176
	s_waitcnt lgkmcnt(0)
	v_lshlrev_b32_e32 v132, 2, v2
	v_lshlrev_b32_e32 v4, 2, v4
	v_mov_b32_e32 v5, v133
	v_lshlrev_b32_e32 v10, 2, v10
	v_mov_b32_e32 v11, v133
	v_lshlrev_b32_e32 v12, 2, v12
	v_mov_b32_e32 v13, v133
	v_lshlrev_b32_e32 v18, 2, v18
	v_mov_b32_e32 v19, v133
	v_lshlrev_b32_e32 v20, 2, v20
	v_mov_b32_e32 v21, v133
	v_lshlrev_b32_e32 v26, 2, v26
	v_mov_b32_e32 v27, v133
	v_lshlrev_b32_e32 v28, 2, v28
	v_mov_b32_e32 v29, v133
	v_lshlrev_b32_e32 v34, 2, v34
	v_mov_b32_e32 v35, v133
	v_lshlrev_b32_e32 v36, 2, v36
	v_mov_b32_e32 v37, v133
	v_lshlrev_b32_e32 v42, 2, v42
	v_mov_b32_e32 v43, v133
	v_lshlrev_b32_e32 v44, 2, v44
	v_mov_b32_e32 v45, v133
	v_lshlrev_b32_e32 v50, 2, v50
	v_mov_b32_e32 v51, v133
	v_lshlrev_b32_e32 v52, 2, v52
	v_mov_b32_e32 v53, v133
	v_lshlrev_b32_e32 v66, 2, v66
	v_mov_b32_e32 v67, v133
	v_lshlrev_b32_e32 v68, 2, v68
	v_mov_b32_e32 v69, v133
	v_lshl_add_u64 v[2:3], s[4:5], 0, v[132:133]
	v_lshlrev_b32_e32 v132, 2, v130
	v_lshl_add_u64 v[4:5], s[4:5], 0, v[4:5]
	v_lshl_add_u64 v[10:11], s[4:5], 0, v[10:11]
	v_lshl_add_u64 v[12:13], s[4:5], 0, v[12:13]
	v_lshl_add_u64 v[18:19], s[4:5], 0, v[18:19]
	v_lshl_add_u64 v[20:21], s[4:5], 0, v[20:21]
	v_lshl_add_u64 v[26:27], s[4:5], 0, v[26:27]
	v_lshl_add_u64 v[28:29], s[4:5], 0, v[28:29]
	v_lshl_add_u64 v[34:35], s[4:5], 0, v[34:35]
	v_lshl_add_u64 v[36:37], s[4:5], 0, v[36:37]
	v_lshl_add_u64 v[42:43], s[4:5], 0, v[42:43]
	v_lshl_add_u64 v[44:45], s[4:5], 0, v[44:45]
	v_lshl_add_u64 v[50:51], s[4:5], 0, v[50:51]
	v_lshl_add_u64 v[52:53], s[4:5], 0, v[52:53]
	v_lshl_add_u64 v[66:67], s[4:5], 0, v[66:67]
	v_lshl_add_u64 v[68:69], s[4:5], 0, v[68:69]
	v_lshl_add_u64 v[2:3], v[2:3], 0, v[132:133]
	v_lshl_add_u64 v[6:7], v[4:5], 0, v[132:133]
	v_lshl_add_u64 v[10:11], v[10:11], 0, v[132:133]
	v_lshl_add_u64 v[14:15], v[12:13], 0, v[132:133]
	v_lshl_add_u64 v[18:19], v[18:19], 0, v[132:133]
	v_lshl_add_u64 v[22:23], v[20:21], 0, v[132:133]
	v_lshl_add_u64 v[26:27], v[26:27], 0, v[132:133]
	v_lshl_add_u64 v[30:31], v[28:29], 0, v[132:133]
	v_lshl_add_u64 v[34:35], v[34:35], 0, v[132:133]
	v_lshl_add_u64 v[38:39], v[36:37], 0, v[132:133]
	v_lshl_add_u64 v[42:43], v[42:43], 0, v[132:133]
	v_lshl_add_u64 v[46:47], v[44:45], 0, v[132:133]
	v_lshl_add_u64 v[50:51], v[50:51], 0, v[132:133]
	v_lshl_add_u64 v[54:55], v[52:53], 0, v[132:133]
	v_lshl_add_u64 v[66:67], v[66:67], 0, v[132:133]
	v_lshl_add_u64 v[70:71], v[68:69], 0, v[132:133]
	global_load_dwordx4 v[2:5], v[2:3], off nt
	s_nop 0
	global_load_dwordx4 v[6:9], v[6:7], off nt
	s_nop 0
	global_load_dwordx4 v[10:13], v[10:11], off nt
	s_nop 0
	global_load_dwordx4 v[14:17], v[14:15], off nt
	s_nop 0
	global_load_dwordx4 v[18:21], v[18:19], off nt
	s_nop 0
	global_load_dwordx4 v[22:25], v[22:23], off nt
	s_nop 0
	global_load_dwordx4 v[26:29], v[26:27], off nt
	s_nop 0
	global_load_dwordx4 v[30:33], v[30:31], off nt
	s_nop 0
	global_load_dwordx4 v[34:37], v[34:35], off nt
	s_nop 0
	global_load_dwordx4 v[38:41], v[38:39], off nt
	s_nop 0
	global_load_dwordx4 v[42:45], v[42:43], off nt
	s_nop 0
	global_load_dwordx4 v[46:49], v[46:47], off nt
	s_nop 0
	global_load_dwordx4 v[50:53], v[50:51], off nt
	s_nop 0
	global_load_dwordx4 v[54:57], v[54:55], off nt
	s_nop 0
	global_load_dwordx4 v[66:69], v[66:67], off nt
	s_nop 0
	global_load_dwordx4 v[70:73], v[70:71], off nt
.LBB0_1769:
	ds_write2_b32 v183, v62, v63 offset1:1
	ds_write2_b32 v184, v64, v65 offset1:1
	ds_write2_b32 v185, v58, v59 offset1:1
	ds_write2_b32 v186, v60, v61 offset1:1
	ds_write2_b32 v187, v78, v79 offset1:1
	ds_write2_b32 v188, v80, v81 offset1:1
	ds_write2_b32 v189, v74, v75 offset1:1
	ds_write2_b32 v190, v76, v77 offset1:1
	ds_write2_b32 v191, v86, v87 offset1:1
	ds_write2_b32 v192, v88, v89 offset1:1
	ds_write2_b32 v193, v82, v83 offset1:1
	ds_write2_b32 v195, v84, v85 offset1:1
	ds_write2_b32 v199, v94, v95 offset1:1
	ds_write2_b32 v201, v96, v97 offset1:1
	ds_write2_b32 v202, v90, v91 offset1:1
	ds_write2_b32 v203, v92, v93 offset1:1
	ds_write2_b32 v204, v102, v103 offset1:1
	ds_write2_b32 v205, v104, v105 offset1:1
	ds_write2_b32 v206, v98, v99 offset1:1
	ds_write2_b32 v207, v100, v101 offset1:1
	ds_write2_b32 v208, v110, v111 offset1:1
	ds_write2_b32 v209, v112, v113 offset1:1
	ds_write2_b32 v210, v106, v107 offset1:1
	ds_write2_b32 v211, v108, v109 offset1:1
	ds_write2_b32 v212, v118, v119 offset1:1
	ds_write2_b32 v213, v120, v121 offset1:1
	ds_write2_b32 v214, v114, v115 offset1:1
	ds_write2_b32 v215, v116, v117 offset1:1
	ds_write2_b32 v216, v126, v127 offset1:1
	ds_write2_b32 v217, v128, v129 offset1:1
	ds_write2_b32 v218, v122, v123 offset1:1
	ds_write2_b32 v219, v124, v125 offset1:1
	s_waitcnt lgkmcnt(0)
	s_waitcnt lgkmcnt(14)
	ds_read_b32 v132, v177 offset:16384
	v_cmp_eq_f32_e64 s[4:5], s57, 0
	s_and_b64 vcc, exec, s[4:5]
	s_cbranch_vccnz .LBB0_1771
	ds_read2_b32 v[154:155], v181 offset0:56 offset1:65
	ds_read2_b32 v[156:157], v181 offset0:121 offset1:130
	ds_read2_b32 v[158:159], v181 offset0:186 offset1:195
	s_waitcnt lgkmcnt(3)
	v_mul_f32_e32 v160, s57, v132
	v_med3_f32 v160, v160, s47, v179
	s_waitcnt lgkmcnt(2)
	v_mul_f32_e32 v155, s57, v155
	v_med3_f32 v155, v155, s47, v179
	v_mov_b32_e32 v184, v133
	v_cvt_pk_fp8_f32 v184, v160, v155
	ds_read2_b32 v[164:165], v182 offset0:123 offset1:132
	ds_read2_b32 v[160:161], v180 offset0:60 offset1:69
	ds_read2_b32 v[162:163], v180 offset0:125 offset1:134
	s_waitcnt lgkmcnt(4)
	v_mul_f32_e32 v157, s57, v157
	s_waitcnt lgkmcnt(3)
	v_mul_f32_e32 v159, s57, v159
	v_med3_f32 v157, v157, s47, v179
	v_med3_f32 v155, v159, s47, v179
	ds_read2_b32 v[168:169], v180 offset0:190 offset1:199
	v_cvt_pk_fp8_f32 v184, v157, v155 op_sel:[0,0,1]
	s_waitcnt lgkmcnt(3)
	v_mul_f32_e32 v155, s57, v165
	s_waitcnt lgkmcnt(2)
	v_mul_f32_e32 v157, s57, v161
	v_med3_f32 v155, v155, s47, v179
	v_med3_f32 v157, v157, s47, v179
	v_mov_b32_e32 v185, v133
	v_cvt_pk_fp8_f32 v185, v155, v157
	s_waitcnt lgkmcnt(1)
	v_mul_f32_e32 v159, s57, v163
	s_waitcnt lgkmcnt(0)
	v_mul_f32_e32 v155, s57, v169
	v_med3_f32 v157, v159, s47, v179
	v_med3_f32 v155, v155, s47, v179
	v_cvt_pk_fp8_f32 v185, v157, v155 op_sel:[0,0,1]
	ds_read2_b32 v[188:189], v181 offset0:8 offset1:16
	ds_read2_b32 v[190:191], v181 offset0:73 offset1:81
	ds_read2_b32 v[192:193], v181 offset0:138 offset1:146
	ds_read2_b32 v[202:203], v181 offset0:203 offset1:211
	v_mov_b64_e32 v[166:167], s[2:3]
	v_mad_u64_u32 v[186:187], s[4:5], s56, v134, v[166:167]
	v_lshl_add_u64 v[186:187], v[186:187], 0, v[136:137]
	s_waitcnt lgkmcnt(3)
	v_mul_f32_e32 v155, s57, v188
	s_waitcnt lgkmcnt(2)
	v_mul_f32_e32 v157, s57, v190
	global_store_dwordx2 v[186:187], v[184:185], off nt
	v_med3_f32 v155, v155, s47, v179
	v_med3_f32 v157, v157, s47, v179
	v_mov_b32_e32 v184, v133
	v_cvt_pk_fp8_f32 v184, v155, v157
	ds_read2_b32 v[186:187], v180 offset0:12 offset1:20
	ds_read2_b32 v[204:205], v180 offset0:77 offset1:85
	ds_read2_b32 v[206:207], v180 offset0:142 offset1:150
	s_waitcnt lgkmcnt(4)
	v_mul_f32_e32 v159, s57, v192
	s_waitcnt lgkmcnt(3)
	v_mul_f32_e32 v161, s57, v202
	v_med3_f32 v159, v159, s47, v179
	v_med3_f32 v155, v161, s47, v179
	ds_read2_b32 v[208:209], v180 offset0:207 offset1:215
	v_cvt_pk_fp8_f32 v184, v159, v155 op_sel:[0,0,1]
	s_waitcnt lgkmcnt(3)
	v_mul_f32_e32 v155, s57, v186
	s_waitcnt lgkmcnt(2)
	v_mul_f32_e32 v157, s57, v204
	v_med3_f32 v155, v155, s47, v179
	v_med3_f32 v157, v157, s47, v179
	v_mov_b32_e32 v185, v133
	v_cvt_pk_fp8_f32 v185, v155, v157
	s_waitcnt lgkmcnt(1)
	v_mul_f32_e32 v159, s57, v206
	s_waitcnt lgkmcnt(0)
	v_mul_f32_e32 v155, s57, v208
	v_med3_f32 v157, v159, s47, v179
	v_med3_f32 v155, v155, s47, v179
	v_cvt_pk_fp8_f32 v185, v157, v155 op_sel:[0,0,1]
	v_mad_u64_u32 v[210:211], s[4:5], s56, v138, v[166:167]
	v_lshl_add_u64 v[210:211], v[210:211], 0, v[136:137]
	v_mul_f32_e32 v155, s57, v189
	v_mul_f32_e32 v157, s57, v191
	global_store_dwordx2 v[210:211], v[184:185], off nt
	v_med3_f32 v155, v155, s47, v179
	v_med3_f32 v157, v157, s47, v179
	v_mov_b32_e32 v184, v133
	v_cvt_pk_fp8_f32 v184, v155, v157
	v_mul_f32_e32 v159, s57, v193
	v_mul_f32_e32 v155, s57, v203
	v_med3_f32 v157, v159, s47, v179
	v_med3_f32 v155, v155, s47, v179
	v_cvt_pk_fp8_f32 v184, v157, v155 op_sel:[0,0,1]
	v_mul_f32_e32 v155, s57, v187
	v_mul_f32_e32 v157, s57, v205
	v_med3_f32 v155, v155, s47, v179
	v_med3_f32 v157, v157, s47, v179
	v_mov_b32_e32 v185, v133
	v_cvt_pk_fp8_f32 v185, v155, v157
	v_mul_f32_e32 v159, s57, v207
	v_mul_f32_e32 v155, s57, v209
	v_med3_f32 v157, v159, s47, v179
	v_med3_f32 v155, v155, s47, v179
	v_cvt_pk_fp8_f32 v185, v157, v155 op_sel:[0,0,1]
	ds_read2_b32 v[188:189], v181 offset0:24 offset1:32
	ds_read2_b32 v[190:191], v181 offset0:89 offset1:97
	ds_read2_b32 v[192:193], v181 offset0:154 offset1:162
	ds_read2_b32 v[202:203], v181 offset0:219 offset1:227
	v_mad_u64_u32 v[186:187], s[4:5], s56, v140, v[166:167]
	v_lshl_add_u64 v[186:187], v[186:187], 0, v[136:137]
	s_waitcnt lgkmcnt(3)
	v_mul_f32_e32 v155, s57, v188
	s_waitcnt lgkmcnt(2)
	v_mul_f32_e32 v157, s57, v190
	global_store_dwordx2 v[186:187], v[184:185], off nt
	v_med3_f32 v155, v155, s47, v179
	v_med3_f32 v157, v157, s47, v179
	v_mov_b32_e32 v184, v133
	v_cvt_pk_fp8_f32 v184, v155, v157
	ds_read2_b32 v[186:187], v180 offset0:28 offset1:36
	ds_read2_b32 v[204:205], v180 offset0:93 offset1:101
	ds_read2_b32 v[206:207], v180 offset0:158 offset1:166
	s_waitcnt lgkmcnt(4)
	v_mul_f32_e32 v159, s57, v192
	s_waitcnt lgkmcnt(3)
	v_mul_f32_e32 v161, s57, v202
	v_med3_f32 v159, v159, s47, v179
	v_med3_f32 v155, v161, s47, v179
	ds_read2_b32 v[208:209], v180 offset0:223 offset1:231
	v_cvt_pk_fp8_f32 v184, v159, v155 op_sel:[0,0,1]
	s_waitcnt lgkmcnt(3)
	v_mul_f32_e32 v155, s57, v186
	s_waitcnt lgkmcnt(2)
	v_mul_f32_e32 v157, s57, v204
	v_med3_f32 v155, v155, s47, v179
	v_med3_f32 v157, v157, s47, v179
	v_mov_b32_e32 v185, v133
	v_cvt_pk_fp8_f32 v185, v155, v157
	s_waitcnt lgkmcnt(1)
	v_mul_f32_e32 v159, s57, v206
	s_waitcnt lgkmcnt(0)
	v_mul_f32_e32 v155, s57, v208
	v_med3_f32 v157, v159, s47, v179
	v_med3_f32 v155, v155, s47, v179
	v_cvt_pk_fp8_f32 v185, v157, v155 op_sel:[0,0,1]
	v_mad_u64_u32 v[210:211], s[4:5], s56, v142, v[166:167]
	v_lshl_add_u64 v[210:211], v[210:211], 0, v[136:137]
	v_mul_f32_e32 v155, s57, v189
	v_mul_f32_e32 v157, s57, v191
	global_store_dwordx2 v[210:211], v[184:185], off nt
	v_med3_f32 v155, v155, s47, v179
	v_med3_f32 v157, v157, s47, v179
	v_mov_b32_e32 v184, v133
	v_cvt_pk_fp8_f32 v184, v155, v157
	v_mul_f32_e32 v159, s57, v193
	v_mul_f32_e32 v155, s57, v203
	v_med3_f32 v157, v159, s47, v179
	v_med3_f32 v155, v155, s47, v179
	v_cvt_pk_fp8_f32 v184, v157, v155 op_sel:[0,0,1]
	v_mul_f32_e32 v155, s57, v187
	v_mul_f32_e32 v157, s57, v205
	v_med3_f32 v155, v155, s47, v179
	v_med3_f32 v157, v157, s47, v179
	v_mov_b32_e32 v185, v133
	v_cvt_pk_fp8_f32 v185, v155, v157
	v_mul_f32_e32 v159, s57, v207
	v_mul_f32_e32 v155, s57, v209
	v_med3_f32 v157, v159, s47, v179
	v_med3_f32 v155, v155, s47, v179
	v_cvt_pk_fp8_f32 v185, v157, v155 op_sel:[0,0,1]
	ds_read2_b32 v[188:189], v181 offset0:40 offset1:48
	ds_read2_b32 v[190:191], v181 offset0:105 offset1:113
	ds_read2_b32 v[192:193], v181 offset0:170 offset1:178
	ds_read2_b32 v[202:203], v181 offset0:235 offset1:243
	v_mad_u64_u32 v[186:187], s[4:5], s56, v144, v[166:167]
	v_lshl_add_u64 v[186:187], v[186:187], 0, v[136:137]
	s_waitcnt lgkmcnt(3)
	v_mul_f32_e32 v155, s57, v188
	s_waitcnt lgkmcnt(2)
	v_mul_f32_e32 v157, s57, v190
	global_store_dwordx2 v[186:187], v[184:185], off nt
	v_med3_f32 v155, v155, s47, v179
	v_med3_f32 v157, v157, s47, v179
	v_mov_b32_e32 v184, v133
	v_cvt_pk_fp8_f32 v184, v155, v157
	ds_read2_b32 v[186:187], v180 offset0:44 offset1:52
	ds_read2_b32 v[204:205], v180 offset0:109 offset1:117
	ds_read2_b32 v[206:207], v180 offset0:174 offset1:182
	s_waitcnt lgkmcnt(4)
	v_mul_f32_e32 v159, s57, v192
	s_waitcnt lgkmcnt(3)
	v_mul_f32_e32 v161, s57, v202
	v_med3_f32 v159, v159, s47, v179
	v_med3_f32 v155, v161, s47, v179
	ds_read2_b32 v[208:209], v180 offset0:239 offset1:247
	v_cvt_pk_fp8_f32 v184, v159, v155 op_sel:[0,0,1]
	s_waitcnt lgkmcnt(3)
	v_mul_f32_e32 v155, s57, v186
	s_waitcnt lgkmcnt(2)
	v_mul_f32_e32 v157, s57, v204
	v_med3_f32 v155, v155, s47, v179
	v_med3_f32 v157, v157, s47, v179
	v_mov_b32_e32 v185, v133
	v_cvt_pk_fp8_f32 v185, v155, v157
	s_waitcnt lgkmcnt(1)
	v_mul_f32_e32 v159, s57, v206
	s_waitcnt lgkmcnt(0)
	v_mul_f32_e32 v155, s57, v208
	v_med3_f32 v157, v159, s47, v179
	v_med3_f32 v155, v155, s47, v179
	v_cvt_pk_fp8_f32 v185, v157, v155 op_sel:[0,0,1]
	v_mad_u64_u32 v[210:211], s[4:5], s56, v146, v[166:167]
	v_lshl_add_u64 v[210:211], v[210:211], 0, v[136:137]
	v_mul_f32_e32 v155, s57, v189
	v_mul_f32_e32 v157, s57, v191
	global_store_dwordx2 v[210:211], v[184:185], off nt
	v_med3_f32 v155, v155, s47, v179
	v_med3_f32 v157, v157, s47, v179
	v_mov_b32_e32 v184, v133
	v_cvt_pk_fp8_f32 v184, v155, v157
	v_mul_f32_e32 v159, s57, v193
	v_mul_f32_e32 v155, s57, v203
	v_med3_f32 v157, v159, s47, v179
	v_med3_f32 v155, v155, s47, v179
	v_cvt_pk_fp8_f32 v184, v157, v155 op_sel:[0,0,1]
	v_mul_f32_e32 v155, s57, v187
	v_mul_f32_e32 v157, s57, v205
	v_med3_f32 v155, v155, s47, v179
	v_med3_f32 v157, v157, s47, v179
	v_mov_b32_e32 v185, v133
	v_cvt_pk_fp8_f32 v185, v155, v157
	v_mul_f32_e32 v159, s57, v207
	v_mul_f32_e32 v155, s57, v209
	v_med3_f32 v157, v159, s47, v179
	v_med3_f32 v155, v155, s47, v179
	v_cvt_pk_fp8_f32 v185, v157, v155 op_sel:[0,0,1]
	v_mul_f32_e32 v154, s57, v154
	v_mul_f32_e32 v155, s57, v156
	v_med3_f32 v157, v154, s47, v179
	v_med3_f32 v155, v155, s47, v179
	v_mov_b32_e32 v154, v133
	v_cvt_pk_fp8_f32 v154, v157, v155
	v_mul_f32_e32 v156, s57, v158
	v_mul_f32_e32 v155, s57, v164
	v_med3_f32 v156, v156, s47, v179
	v_med3_f32 v155, v155, s47, v179
	ds_read_b32 v158, v177 offset:18428
	v_cvt_pk_fp8_f32 v154, v156, v155 op_sel:[0,0,1]
	v_mul_f32_e32 v155, s57, v160
	v_mul_f32_e32 v156, s57, v162
	v_med3_f32 v159, v155, s47, v179
	v_med3_f32 v156, v156, s47, v179
	v_mov_b32_e32 v155, v133
	v_cvt_pk_fp8_f32 v155, v159, v156
	v_mul_f32_e32 v157, s57, v168
	s_waitcnt lgkmcnt(0)
	v_mul_f32_e32 v156, s57, v158
	v_med3_f32 v157, v157, s47, v179
	v_med3_f32 v156, v156, s47, v179
	v_cvt_pk_fp8_f32 v155, v157, v156 op_sel:[0,0,1]
	v_mad_u64_u32 v[186:187], s[4:5], s56, v148, v[166:167]
	v_mad_u64_u32 v[156:157], s[4:5], s56, v150, v[166:167]
	v_lshl_add_u64 v[186:187], v[186:187], 0, v[136:137]
	v_lshl_add_u64 v[156:157], v[156:157], 0, v[136:137]
	global_store_dwordx2 v[186:187], v[184:185], off nt
	global_store_dwordx2 v[156:157], v[154:155], off nt
	s_cbranch_execnz .LBB0_1701
	s_branch .LBB0_1700
